# hand-written fp8 weight-conversion helper loop (3-buffer pipeline, counted vmcnt, LDS gain table); 73 helper WGs in phase 1, more MoE weight items moved from phase 0 to the helpers
# speedup vs baseline: 1.0235x; 1.0212x over previous
; #define GAS __attribute__((address_space(1)))
; __device__ __forceinline__ unsigned pk2(float lo, float hi) { return f2bf(lo) | (f2bf(hi) << 16); }
; __device__ __forceinline__ void row_to_bf16(const float* xrow, bf16* orow, float* ss, int lane) {
;     const GAS f32x4* xr = (const GAS f32x4*)xrow + lane; float s = 0.f;
;     GAS v2u* o8 = (GAS v2u*)orow + lane;
; #pragma unroll
;     for (int j = 0; j < 8; ++j) { const f32x4 v = xr[64 * j]; s += (v.x * v.x + v.y * v.y) + (v.z * v.z + v.w * v.w); v2u w; w.x = pk2(v.x, v.y); w.y = pk2(v.z, v.w); o8[64 * j] = w; }
;     s = wave_sum(s); if (lane == 0) *ss = s;
; }
; __device__ __forceinline__ void p0_rows(const P& p, int gw, int NGW, int lane) {
;     unsigned char* ws = p.ws;
;     for (int m = gw; m < NTOK; m += NGW) row_to_bf16(p.x + (size_t)m * DM, (bf16*)(ws + WS_XB) + (size_t)m * DM, (float*)(ws + WS_SS0) + m, lane);
;     for (int m = gw; m < NMEM; m += NGW) row_to_bf16(p.mem + (size_t)m * DM, (bf16*)(ws + WS_MEMB) + (size_t)m * DM, (float*)(ws + WS_SSM) + m, lane);
;     for (int i = gw * 64 + lane; i < NE * DM; i += NGW * 64) { const int e = i >> 11, k = i & 2047; ((float*)(ws + WS_W_R))[i] = p.g_ffn[k] * p.w_r[k * NE + e]; }
; }
; __global__ void __launch_bounds__(NWAVES * 64, 2) fwd(P p) {
;     ...
;     const int GP1 = (G == 256) ? G - NHELP : G, p0_last = (G == 256) ? P0_SPLIT : P0_NITEMS;
.LBB5_15:
	v_writelane_b32 v253, s0, 59
	s_mov_b32 s0, s16
	v_writelane_b32 v253, s0, 60
	s_lshr_b32 s95, s16, 6
	s_lshl_b32 s26, s33, 3
	v_writelane_b32 v253, s1, 61
	s_lshl_b32 s0, s94, 3
	s_add_i32 s28, s0, s95
	s_cmpk_lg_i32 s33, 0x100
	s_cselect_b64 s[0:1], -1, 0
	s_cmpk_eq_i32 s33, 0x100
	v_writelane_b32 v253, s0, 62
	s_cselect_b64 s[80:81], -1, 0
	s_mov_b32 s3, 0x40a0
	v_writelane_b32 v253, s1, 63
	s_and_b64 s[0:1], s[80:81], exec
	s_cselect_b32 s3, s3, 0x1a480
	s_cmp_lt_i32 s24, 1
	s_cselect_b64 s[56:57], -1, 0
	s_cmp_gt_i32 s24, 0
	s_cselect_b64 s[0:1], -1, 0
	s_cmp_lt_i32 s25, 1
	s_cselect_b64 s[4:5], -1, 0
	s_or_b64 s[0:1], s[0:1], s[4:5]
	v_and_b32_e32 v198, 63, v0
	s_and_b64 vcc, exec, s[0:1]
	s_cbranch_vccnz .LBB5_387
	s_cmpk_gt_i32 s28, 0x7fff
	s_movk_i32 s4, 0x7fff
	s_cbranch_scc1 .LBB5_21
	v_mbcnt_lo_u32_b32 v1, -1, 0
	v_mbcnt_hi_u32_b32 v2, -1, v1
	v_and_b32_e32 v1, 64, v2
	v_add_u32_e32 v3, 64, v1
	v_xor_b32_e32 v1, 1, v2
	v_cmp_lt_i32_e32 vcc, v1, v3
	v_xor_b32_e32 v4, 2, v2
	s_ashr_i32 s29, s28, 31
	v_cndmask_b32_e32 v1, v2, v1, vcc
	v_cmp_lt_i32_e32 vcc, v4, v3
	s_lshl_b64 s[0:1], s[28:29], 2
	s_add_u32 s5, s0, 0x2700000
	v_cndmask_b32_e32 v4, v2, v4, vcc
	v_lshlrev_b32_e32 v10, 2, v4
	v_xor_b32_e32 v4, 4, v2
	v_cmp_lt_i32_e32 vcc, v4, v3
	s_addc_u32 s6, s1, 0
	s_ashr_i32 s27, s26, 31
	v_cndmask_b32_e32 v4, v2, v4, vcc
	v_lshlrev_b32_e32 v11, 2, v4
	v_xor_b32_e32 v4, 8, v2
	v_cmp_lt_i32_e32 vcc, v4, v3
	s_lshl_b64 s[0:1], s[28:29], 12
	s_lshl_b64 s[34:35], s[26:27], 2
	v_cndmask_b32_e32 v4, v2, v4, vcc
	v_lshlrev_b32_e32 v12, 2, v4
	v_xor_b32_e32 v4, 16, v2
	v_cmp_lt_i32_e32 vcc, v4, v3
	s_lshl_b64 s[68:69], s[26:27], 12
	v_readlane_b32 s36, v253, 10
	v_cndmask_b32_e32 v4, v2, v4, vcc
	v_lshlrev_b32_e32 v13, 2, v4
	v_xor_b32_e32 v4, 32, v2
	v_cmp_lt_i32_e32 vcc, v4, v3
	v_mov_b32_e32 v3, s1
	v_readlane_b32 s37, v253, 11
	v_cndmask_b32_e32 v2, v2, v4, vcc
	v_lshlrev_b32_e32 v14, 2, v2
	v_lshl_or_b32 v2, v198, 3, s0
	s_lshl_b64 s[0:1], s[28:29], 13
	s_add_u32 s0, s36, s0
	v_lshlrev_b32_e32 v4, 4, v198
	v_mov_b32_e32 v5, 0
	s_addc_u32 s1, s37, s1
	v_lshl_add_u64 v[6:7], s[0:1], 0, v[4:5]
	s_mov_b64 s[0:1], 0x1000
	v_lshlrev_b32_e32 v1, 2, v1
	v_cmp_eq_u32_e32 vcc, 0, v198
	v_lshl_add_u64 v[6:7], v[6:7], 0, s[0:1]
	s_lshl_b64 s[36:37], s[26:27], 13
	s_brev_b32 s7, 28
	v_mov_b32_e32 v4, 1
	s_mov_b32 s8, s28
	v_readlane_b32 s38, v253, 12
	v_readlane_b32 s39, v253, 13
	v_readlane_b32 s40, v253, 14
	v_readlane_b32 s41, v253, 15
	v_readlane_b32 s42, v253, 16
	v_readlane_b32 s43, v253, 17
	v_readlane_b32 s44, v253, 18
	v_readlane_b32 s45, v253, 19
	v_readlane_b32 s46, v253, 20
	v_readlane_b32 s47, v253, 21
	v_readlane_b32 s48, v253, 22
	v_readlane_b32 s49, v253, 23
	v_readlane_b32 s50, v253, 24
	v_readlane_b32 s51, v253, 25
	s_branch .LBB5_19

; #define LAS __attribute__((address_space(3)))
; __device__ __forceinline__ void p0_items(const P& p, LAS unsigned char* lds, int first, int last, int gw, int NGW, int wave, int lane) {
;     LAS float* scr = (LAS float*)(lds + wave * 16384);
;     unsigned char* ws = p.ws;
;     constexpr int I_IN = P0_I_IN, I_OUT = P0_I_OUT, I_CQ = P0_I_CQ, I_CKV = P0_I_CKV, I_CO = P0_I_CO, I_G = P0_I_G, I_GU = P0_I_GU;
;     ...
;     const int it0 = first + gw, st = NGW;
;     if (it0 < last) {
;         TrItem d0, d1, d2; f32x4 v0[16], v1[16], v2[16];
;         P0_DESC(d0, it0); tr_load(d0, v0, lane); d1 = d0; d2 = d0;
;         if (it0 + st < last) { P0_DESC(d1, it0 + st); tr_load(d1, v1, lane); }
;         for (int it = it0; it < last; it += 3 * st) {
;             if (it + 2 * st < last) { P0_DESC(d2, it + 2 * st); tr_load(d2, v2, lane); }
;             tr_finish(d0, v0, scr, lane);
;             if (it + st >= last) break;
;             if (it + 3 * st < last) { P0_DESC(d0, it + 3 * st); tr_load(d0, v0, lane); }
;             tr_finish(d1, v1, scr, lane);
;             if (it + 2 * st >= last) break;
;             if (it + 4 * st < last) { P0_DESC(d1, it + 4 * st); tr_load(d1, v1, lane); }
;             tr_finish(d2, v2, scr, lane);
;         }
;     }
; __global__ void __launch_bounds__(NWAVES * 64, 2) fwd(P p) {
;     ...
;     const int GP1 = (G == 256) ? G - NHELP : G, p0_last = (G == 256) ? P0_SPLIT : P0_NITEMS;
.LBB5_437:
	s_cmp_lt_i32 s24, 2
	s_cselect_b64 s[44:45], -1, 0
	s_and_b64 s[0:1], s[44:45], s[0:1]
	s_andn2_b64 vcc, exec, s[0:1]
	s_cbranch_vccnz .LBB5_819
	s_and_b64 s[0:1], s[80:81], exec
	s_cselect_b32 s27, 0xb7, s33
	s_cmp_ge_i32 s2, s27
	s_mov_b64 s[0:1], -1
	s_cbranch_scc0 .LBB5_767
	s_sub_i32 s0, s2, s27
	v_writelane_b32 v252, s44, 4
	s_lshl_b32 s0, s0, 3
	s_add_i32 s5, s3, s95
	v_writelane_b32 v252, s45, 5
	s_add_i32 s4, s5, s0
	v_writelane_b32 v252, s94, 22
	s_nop 0
	v_writelane_b32 v252, s95, 23
	v_readlane_b32 s50, v253, 50
	v_readlane_b32 s51, v253, 51
	v_readlane_b32 s12, v253, 56
	v_readlane_b32 s13, v253, 57
	v_readlane_b32 s14, v253, 4
	v_readlane_b32 s15, v253, 5
	s_sub_i32 s5, s33, s27
	s_lshl_b32 s5, s5, 3
	s_mov_b32 s6, 0x1a480
	s_lshl_b32 s59, s5, 1
	s_add_i32 s60, s59, s5
	s_lshl_b32 s61, s5, 2
	s_add_u32 s16, s22, 0x8000000
	s_addc_u32 s17, s23, 0
	s_add_u32 s18, s22, 0x28000000
	s_addc_u32 s19, s23, 0
	s_lshl_b32 s58, s95, 14
	v_lshlrev_b32_e32 v1, 4, v0
	global_load_dwordx4 v[4:7], v1, s[50:51]
	v_and_b32_e32 v2, 7, v0
	v_bfe_u32 v3, v0, 3, 3
	v_lshlrev_b32_e32 v200, 4, v2
	v_lshl_add_u32 v201, v3, 13, v200
	v_lshl_add_u32 v200, v3, 14, v200
	v_lshlrev_b32_e32 v202, 6, v2
	v_lshl_add_u32 v211, v3, 7, s58
	v_xor_b32_e32 v242, 0, v2
	v_lshl_add_u32 v203, v242, 4, v211
	v_xor_b32_e32 v242, 1, v2
	v_lshl_add_u32 v204, v242, 4, v211
	v_xor_b32_e32 v242, 2, v2
	v_lshl_add_u32 v205, v242, 4, v211
	v_xor_b32_e32 v242, 3, v2
	v_lshl_add_u32 v206, v242, 4, v211
	v_xor_b32_e32 v242, 4, v2
	v_lshl_add_u32 v207, v242, 4, v211
	v_xor_b32_e32 v242, 5, v2
	v_lshl_add_u32 v208, v242, 4, v211
	v_xor_b32_e32 v242, 6, v2
	v_lshl_add_u32 v209, v242, 4, v211
	v_xor_b32_e32 v242, 7, v2
	v_lshl_add_u32 v210, v242, 4, v211
	v_lshl_add_u32 v211, v2, 11, s58
	v_and_b32_e32 v242, 3, v3
	v_lshl_add_u32 v211, v242, 2, v211
	v_lshrrev_b32_e32 v243, 2, v3
	v_add_u32_e32 v242, 0, v243
	v_xor_b32_e32 v242, v242, v2
	v_lshl_add_u32 v230, v242, 4, v211
	v_add_u32_e32 v234, 0x400, v230
	v_add_u32_e32 v242, 2, v243
	v_xor_b32_e32 v242, v242, v2
	v_lshl_add_u32 v231, v242, 4, v211
	v_add_u32_e32 v235, 0x400, v231
	v_add_u32_e32 v242, 4, v243
	v_xor_b32_e32 v242, v242, v2
	v_lshl_add_u32 v232, v242, 4, v211
	v_add_u32_e32 v236, 0x400, v232
	v_add_u32_e32 v242, 6, v243
	v_xor_b32_e32 v242, v242, v2
	v_lshl_add_u32 v233, v242, 4, v211
	v_add_u32_e32 v237, 0x400, v233
	v_lshlrev_b32_e32 v242, 4, v2
	v_lshl_add_u32 v238, v3, 11, v242
	v_add_u32_e32 v239, 0x4000, v238
	v_add_u32_e32 v240, 0x8000, v238
	v_add_u32_e32 v241, 0xc000, v238
	s_waitcnt vmcnt(0)
	v_mul_f32_e32 v4, 0x42800000, v4
	v_mul_f32_e32 v5, 0x42800000, v5
	v_mul_f32_e32 v6, 0x42800000, v6
	v_mul_f32_e32 v7, 0x42800000, v7
	v_add_u32_e32 v2, 0x21800, v1
	ds_write_b128 v2, v[4:7]
	v_and_b32_e32 v2, 48, v1
	v_add_u32_e32 v2, 0x23800, v2
	v_mov_b32_e32 v8, 0x42800000
	v_mov_b32_e32 v9, 0x42800000
	v_mov_b32_e32 v10, 0x42800000
	v_mov_b32_e32 v11, 0x42800000
	ds_write_b128 v2, v[8:11]
	s_waitcnt lgkmcnt(0)
	s_barrier
	s_cmp_lt_u32 s4, s6
	s_cbranch_scc0 .Lhlp_done
	s_sub_i32 s50, s4, 0x2480
	s_cmp_lt_u32 s50, 0x10000
	s_cbranch_scc0 .Lhlp_dn_p0
	s_lshr_b32 s51, s50, 11
	s_bfe_u32 s52, s50, 0x40007
	s_and_b32 s53, s50, 0x7f
	s_lshl_b32 s54, s53, 5
	s_lshl_b32 s55, s51, 25
	s_lshl_b32 s56, s52, 21
	s_add_u32 s55, s55, s56
	s_lshl_b32 s56, s54, 2
	s_add_u32 s55, s55, s56
	s_add_u32 s8, s12, s55
	s_addc_u32 s9, s13, 0
	s_mov_b32 s10, 0x20000
	s_bfe_u32 s56, s53, 0x40002
	s_lshl_b32 s56, s56, 8
	s_and_b32 s57, s53, 3
	s_lshl_b32 s57, s57, 5
	s_add_u32 s56, s56, s57
	s_lshr_b32 s57, s53, 6
	s_lshl_b32 s57, s57, 7
	s_add_u32 s56, s56, s57
	s_lshl_b32 s56, s56, 11
	s_lshl_b32 s57, s51, 23
	s_add_u32 s56, s56, s57
	s_lshl_b32 s57, s52, 7
	s_add_u32 s56, s56, s57
	s_add_u32 s34, s16, s56
	s_addc_u32 s35, s17, 0
	s_lshl_b32 s57, s52, 9
	s_add_u32 s36, s57, 0x21800
	s_mov_b32 s37, -1
	v_mov_b32_e32 v211, v200
	s_branch .Lhlp_ld_p0
.Lhlp_dn_p0:
	s_sub_i32 s50, s50, 0x10000
	s_lshr_b32 s51, s50, 10
	s_bfe_u32 s52, s50, 0x40006
	s_and_b32 s53, s50, 63
	s_lshl_b32 s54, s53, 5
	s_lshl_b32 s55, s51, 24
	s_lshl_b32 s56, s52, 20
	s_add_u32 s55, s55, s56
	s_lshl_b32 s56, s54, 2
	s_add_u32 s55, s55, s56
	s_add_u32 s8, s14, s55
	s_addc_u32 s9, s15, 0
	s_mov_b32 s10, 0x10000
	s_lshl_b32 s56, s51, 22
	s_lshl_b32 s57, s54, 11
	s_add_u32 s56, s56, s57
	s_lshl_b32 s57, s52, 7
	s_add_u32 s56, s56, s57
	s_add_u32 s34, s18, s56
	s_addc_u32 s35, s19, 0
	s_mov_b32 s36, 0x23800
	s_mov_b32 s37, 0
	v_mov_b32_e32 v211, v201
.Lhlp_ld_p0:
	global_load_dwordx4 v[4:7], v211, s[8:9] nt
	v_add_u32_e32 v211, s10, v211
	global_load_dwordx4 v[8:11], v211, s[8:9] nt
	v_add_u32_e32 v211, s10, v211
	global_load_dwordx4 v[12:15], v211, s[8:9] nt
	v_add_u32_e32 v211, s10, v211
	global_load_dwordx4 v[16:19], v211, s[8:9] nt
	v_add_u32_e32 v211, s10, v211
	global_load_dwordx4 v[20:23], v211, s[8:9] nt
	v_add_u32_e32 v211, s10, v211
	global_load_dwordx4 v[24:27], v211, s[8:9] nt
	v_add_u32_e32 v211, s10, v211
	global_load_dwordx4 v[28:31], v211, s[8:9] nt
	v_add_u32_e32 v211, s10, v211
	global_load_dwordx4 v[32:35], v211, s[8:9] nt
	v_add_u32_e32 v211, s10, v211
	global_load_dwordx4 v[36:39], v211, s[8:9] nt
	v_add_u32_e32 v211, s10, v211
	global_load_dwordx4 v[40:43], v211, s[8:9] nt
	v_add_u32_e32 v211, s10, v211
	global_load_dwordx4 v[44:47], v211, s[8:9] nt
	v_add_u32_e32 v211, s10, v211
	global_load_dwordx4 v[48:51], v211, s[8:9] nt
	v_add_u32_e32 v211, s10, v211
	global_load_dwordx4 v[52:55], v211, s[8:9] nt
	v_add_u32_e32 v211, s10, v211
	global_load_dwordx4 v[56:59], v211, s[8:9] nt
	v_add_u32_e32 v211, s10, v211
	global_load_dwordx4 v[60:63], v211, s[8:9] nt
	v_add_u32_e32 v211, s10, v211
	global_load_dwordx4 v[64:67], v211, s[8:9] nt
	s_add_i32 s7, s4, s5
	s_cmp_lt_u32 s7, s6
	s_cbranch_scc0 .Lhlp_loop
	s_sub_i32 s50, s7, 0x2480
	s_cmp_lt_u32 s50, 0x10000
	s_cbranch_scc0 .Lhlp_dn_p1
	s_lshr_b32 s51, s50, 11
	s_bfe_u32 s52, s50, 0x40007
	s_and_b32 s53, s50, 0x7f
	s_lshl_b32 s54, s53, 5
	s_lshl_b32 s55, s51, 25
	s_lshl_b32 s56, s52, 21
	s_add_u32 s55, s55, s56
	s_lshl_b32 s56, s54, 2
	s_add_u32 s55, s55, s56
	s_add_u32 s8, s12, s55
	s_addc_u32 s9, s13, 0
	s_mov_b32 s10, 0x20000
	s_bfe_u32 s56, s53, 0x40002
	s_lshl_b32 s56, s56, 8
	s_and_b32 s57, s53, 3
	s_lshl_b32 s57, s57, 5
	s_add_u32 s56, s56, s57
	s_lshr_b32 s57, s53, 6
	s_lshl_b32 s57, s57, 7
	s_add_u32 s56, s56, s57
	s_lshl_b32 s56, s56, 11
	s_lshl_b32 s57, s51, 23
	s_add_u32 s56, s56, s57
	s_lshl_b32 s57, s52, 7
	s_add_u32 s56, s56, s57
	s_add_u32 s38, s16, s56
	s_addc_u32 s39, s17, 0
	s_lshl_b32 s57, s52, 9
	s_add_u32 s40, s57, 0x21800
	s_mov_b32 s41, -1
	v_mov_b32_e32 v211, v200
	s_branch .Lhlp_ld_p1
; #define GAS __attribute__((address_space(1)))
; __device__ __forceinline__ void tr_load(const TrItem& d, f32x4 (&v)[16], int lane) {
;     const int g = lane & 7, r0 = lane >> 3;
; #pragma unroll
;     for (int i = 0; i < 8; ++i) v[i] = __builtin_nontemporal_load((const GAS f32x4*)(d.W + (size_t)(d.k0 + r0 + 8 * i) * d.N + d.n0 + 4 * g));
;     if (d.is8) {
; #pragma unroll
;         for (int i = 8; i < 16; ++i) v[i] = __builtin_nontemporal_load((const GAS f32x4*)(d.W + (size_t)(d.k0 + r0 + 8 * i) * d.N + d.n0 + 4 * g)); }
; }
; __device__ __forceinline__ void p0_items(const P& p, LAS unsigned char* lds, int first, int last, int gw, int NGW, int wave, int lane) {
;     ...
;     const int it0 = first + gw, st = NGW;
;     if (it0 < last) {
;         TrItem d0, d1, d2; f32x4 v0[16], v1[16], v2[16];
;         P0_DESC(d0, it0); tr_load(d0, v0, lane); d1 = d0; d2 = d0;
;         if (it0 + st < last) { P0_DESC(d1, it0 + st); tr_load(d1, v1, lane); }
;         for (int it = it0; it < last; it += 3 * st) {
;             if (it + 2 * st < last) { P0_DESC(d2, it + 2 * st); tr_load(d2, v2, lane); }
.Lhlp_dn_p1:
	s_sub_i32 s50, s50, 0x10000
	s_lshr_b32 s51, s50, 10
	s_bfe_u32 s52, s50, 0x40006
	s_and_b32 s53, s50, 63
	s_lshl_b32 s54, s53, 5
	s_lshl_b32 s55, s51, 24
	s_lshl_b32 s56, s52, 20
	s_add_u32 s55, s55, s56
	s_lshl_b32 s56, s54, 2
	s_add_u32 s55, s55, s56
	s_add_u32 s8, s14, s55
	s_addc_u32 s9, s15, 0
	s_mov_b32 s10, 0x10000
	s_lshl_b32 s56, s51, 22
	s_lshl_b32 s57, s54, 11
	s_add_u32 s56, s56, s57
	s_lshl_b32 s57, s52, 7
	s_add_u32 s56, s56, s57
	s_add_u32 s38, s18, s56
	s_addc_u32 s39, s19, 0
	s_mov_b32 s40, 0x23800
	s_mov_b32 s41, 0
	v_mov_b32_e32 v211, v201
.Lhlp_ld_p1:
	global_load_dwordx4 v[68:71], v211, s[8:9] nt
	v_add_u32_e32 v211, s10, v211
	global_load_dwordx4 v[72:75], v211, s[8:9] nt
	v_add_u32_e32 v211, s10, v211
	global_load_dwordx4 v[76:79], v211, s[8:9] nt
	v_add_u32_e32 v211, s10, v211
	global_load_dwordx4 v[80:83], v211, s[8:9] nt
	v_add_u32_e32 v211, s10, v211
	global_load_dwordx4 v[84:87], v211, s[8:9] nt
	v_add_u32_e32 v211, s10, v211
	global_load_dwordx4 v[88:91], v211, s[8:9] nt
	v_add_u32_e32 v211, s10, v211
	global_load_dwordx4 v[92:95], v211, s[8:9] nt
	v_add_u32_e32 v211, s10, v211
	global_load_dwordx4 v[96:99], v211, s[8:9] nt
	v_add_u32_e32 v211, s10, v211
	global_load_dwordx4 v[100:103], v211, s[8:9] nt
	v_add_u32_e32 v211, s10, v211
	global_load_dwordx4 v[104:107], v211, s[8:9] nt
	v_add_u32_e32 v211, s10, v211
	global_load_dwordx4 v[108:111], v211, s[8:9] nt
	v_add_u32_e32 v211, s10, v211
	global_load_dwordx4 v[112:115], v211, s[8:9] nt
	v_add_u32_e32 v211, s10, v211
	global_load_dwordx4 v[116:119], v211, s[8:9] nt
	v_add_u32_e32 v211, s10, v211
	global_load_dwordx4 v[120:123], v211, s[8:9] nt
	v_add_u32_e32 v211, s10, v211
	global_load_dwordx4 v[124:127], v211, s[8:9] nt
	v_add_u32_e32 v211, s10, v211
	global_load_dwordx4 v[128:131], v211, s[8:9] nt
.Lhlp_loop:
	s_add_i32 s7, s4, s59
	s_cmp_lt_u32 s7, s6
	s_cbranch_scc0 .Lhlp_skip_0
	s_sub_i32 s50, s7, 0x2480
	s_cmp_lt_u32 s50, 0x10000
	s_cbranch_scc0 .Lhlp_dn_k0
	s_lshr_b32 s51, s50, 11
	s_bfe_u32 s52, s50, 0x40007
	s_and_b32 s53, s50, 0x7f
	s_lshl_b32 s54, s53, 5
	s_lshl_b32 s55, s51, 25
	s_lshl_b32 s56, s52, 21
	s_add_u32 s55, s55, s56
	s_lshl_b32 s56, s54, 2
	s_add_u32 s55, s55, s56
	s_add_u32 s8, s12, s55
	s_addc_u32 s9, s13, 0
	s_mov_b32 s10, 0x20000
	s_bfe_u32 s56, s53, 0x40002
	s_lshl_b32 s56, s56, 8
	s_and_b32 s57, s53, 3
	s_lshl_b32 s57, s57, 5
	s_add_u32 s56, s56, s57
	s_lshr_b32 s57, s53, 6
	s_lshl_b32 s57, s57, 7
	s_add_u32 s56, s56, s57
	s_lshl_b32 s56, s56, 11
	s_lshl_b32 s57, s51, 23
	s_add_u32 s56, s56, s57
	s_lshl_b32 s57, s52, 7
	s_add_u32 s56, s56, s57
	s_add_u32 s46, s16, s56
	s_addc_u32 s47, s17, 0
	s_lshl_b32 s57, s52, 9
	s_add_u32 s48, s57, 0x21800
	s_mov_b32 s49, -1
	v_mov_b32_e32 v211, v200
	s_branch .Lhlp_ld_k0
.Lhlp_dn_k0:
	s_sub_i32 s50, s50, 0x10000
	s_lshr_b32 s51, s50, 10
	s_bfe_u32 s52, s50, 0x40006
	s_and_b32 s53, s50, 63
	s_lshl_b32 s54, s53, 5
	s_lshl_b32 s55, s51, 24
	s_lshl_b32 s56, s52, 20
	s_add_u32 s55, s55, s56
	s_lshl_b32 s56, s54, 2
	s_add_u32 s55, s55, s56
	s_add_u32 s8, s14, s55
	s_addc_u32 s9, s15, 0
	s_mov_b32 s10, 0x10000
	s_lshl_b32 s56, s51, 22
	s_lshl_b32 s57, s54, 11
	s_add_u32 s56, s56, s57
	s_lshl_b32 s57, s52, 7
	s_add_u32 s56, s56, s57
	s_add_u32 s46, s18, s56
	s_addc_u32 s47, s19, 0
	s_mov_b32 s48, 0x23800
	s_mov_b32 s49, 0
	v_mov_b32_e32 v211, v201
.Lhlp_ld_k0:
	global_load_dwordx4 v[132:135], v211, s[8:9] nt
	v_add_u32_e32 v211, s10, v211
	global_load_dwordx4 v[136:139], v211, s[8:9] nt
	v_add_u32_e32 v211, s10, v211
	global_load_dwordx4 v[140:143], v211, s[8:9] nt
	v_add_u32_e32 v211, s10, v211
	global_load_dwordx4 v[144:147], v211, s[8:9] nt
	v_add_u32_e32 v211, s10, v211
	global_load_dwordx4 v[148:151], v211, s[8:9] nt
	v_add_u32_e32 v211, s10, v211
	global_load_dwordx4 v[152:155], v211, s[8:9] nt
	v_add_u32_e32 v211, s10, v211
	global_load_dwordx4 v[156:159], v211, s[8:9] nt
	v_add_u32_e32 v211, s10, v211
	global_load_dwordx4 v[160:163], v211, s[8:9] nt
	v_add_u32_e32 v211, s10, v211
	global_load_dwordx4 v[164:167], v211, s[8:9] nt
	v_add_u32_e32 v211, s10, v211
	global_load_dwordx4 v[168:171], v211, s[8:9] nt
	v_add_u32_e32 v211, s10, v211
	global_load_dwordx4 v[172:175], v211, s[8:9] nt
	v_add_u32_e32 v211, s10, v211
	global_load_dwordx4 v[176:179], v211, s[8:9] nt
	v_add_u32_e32 v211, s10, v211
	global_load_dwordx4 v[180:183], v211, s[8:9] nt
	v_add_u32_e32 v211, s10, v211
	global_load_dwordx4 v[184:187], v211, s[8:9] nt
	v_add_u32_e32 v211, s10, v211
	global_load_dwordx4 v[188:191], v211, s[8:9] nt
	v_add_u32_e32 v211, s10, v211
	global_load_dwordx4 v[192:195], v211, s[8:9] nt
	s_branch .Lhlp_fin_0

; #define GAS __attribute__((address_space(1)))
; #define LAS __attribute__((address_space(3)))
; __device__ __forceinline__ unsigned pk4_fp8(float a, float b, float c, float d) { int w = 0; w = __builtin_amdgcn_cvt_pk_fp8_f32(a, b, w, false); w = __builtin_amdgcn_cvt_pk_fp8_f32(c, d, w, true); return (unsigned)w; }
; #define LDS_WAIT() asm volatile("s_waitcnt lgkmcnt(0)" ::: "memory")
; __device__ __forceinline__ void tr_finish(const TrItem& d, const f32x4 (&v)[16], LAS float* scr, int lane_) {
;     int lane = lane_; asm volatile("" : "+v"(lane));
;     const int c = lane & 7;
;     if (d.is8) {
;         { const int g = lane & 7, r0 = lane >> 3;
; #pragma unroll
;           for (int i = 0; i < 16; ++i) { const float gs = (d.gain ? d.gain[d.k0 + r0 + 8 * i] : 1.0f) * W8_SCALE; *(LAS f32x4*)(scr + (r0 + 8 * i) * 32 + ((g ^ (i >> 1)) << 2)) = v[i] * gs;
;               if ((i & 3) == 3) asm volatile("" ::: "memory"); } }
;         LDS_WAIT(); asm volatile("" ::: "memory");
; #pragma unroll
;         for (int j = 0; j < 4; ++j) { const int n = (lane >> 3) + 8 * j; const LAS float* s = scr + (16 * c) * 32 + ((((n >> 2) ^ c) << 2) + (n & 3));
;             v4u o; o.x = pk4_fp8(s[0 * 32], s[1 * 32], s[2 * 32], s[3 * 32]); o.y = pk4_fp8(s[4 * 32], s[5 * 32], s[6 * 32], s[7 * 32]); o.z = pk4_fp8(s[8 * 32], s[9 * 32], s[10 * 32], s[11 * 32]); o.w = pk4_fp8(s[12 * 32], s[13 * 32], s[14 * 32], s[15 * 32]);
;             __builtin_nontemporal_store(o, (GAS v4u*)(d.WT + (size_t)(d.drow0 + n) * d.K + d.k0 + 16 * c)); }
; __device__ __forceinline__ void p0_items(const P& p, LAS unsigned char* lds, int first, int last, int gw, int NGW, int wave, int lane) {
;     ...
;         for (int it = it0; it < last; it += 3 * st) {
;             if (it + 2 * st < last) { P0_DESC(d2, it + 2 * st); tr_load(d2, v2, lane); }
;             tr_finish(d0, v0, scr, lane);
;             if (it + st >= last) break;
;             if (it + 3 * st < last) { P0_DESC(d0, it + 3 * st); tr_load(d0, v0, lane); }
;             tr_finish(d1, v1, scr, lane);
.Lhlp_fin_0:
	s_waitcnt vmcnt(32)
	ds_write_b128 v203, v[4:7]
	ds_write_b128 v203, v[8:11] offset:1024
	ds_write_b128 v204, v[12:15] offset:2048
	ds_write_b128 v204, v[16:19] offset:3072
	ds_write_b128 v205, v[20:23] offset:4096
	ds_write_b128 v205, v[24:27] offset:5120
	ds_write_b128 v206, v[28:31] offset:6144
	ds_write_b128 v206, v[32:35] offset:7168
	ds_write_b128 v207, v[36:39] offset:8192
	ds_write_b128 v207, v[40:43] offset:9216
	ds_write_b128 v208, v[44:47] offset:10240
	ds_write_b128 v208, v[48:51] offset:11264
	ds_write_b128 v209, v[52:55] offset:12288
	ds_write_b128 v209, v[56:59] offset:13312
	ds_write_b128 v210, v[60:63] offset:14336
	ds_write_b128 v210, v[64:67] offset:15360
	v_and_b32_e32 v242, s37, v202
	v_add_u32_e32 v242, s36, v242
	s_waitcnt lgkmcnt(0)
	ds_read_b128 v[214:217], v242
	ds_read_b128 v[218:221], v242 offset:16
	ds_read_b128 v[222:225], v242 offset:32
	ds_read_b128 v[226:229], v242 offset:48
	ds_read2_b32 v[4:5], v230 offset1:32
	ds_read2_b32 v[6:7], v230 offset0:64 offset1:96
	ds_read2_b32 v[8:9], v230 offset0:128 offset1:160
	ds_read2_b32 v[10:11], v230 offset0:192 offset1:224
	ds_read2_b32 v[12:13], v234 offset1:32
	ds_read2_b32 v[14:15], v234 offset0:64 offset1:96
	ds_read2_b32 v[16:17], v234 offset0:128 offset1:160
	ds_read2_b32 v[18:19], v234 offset0:192 offset1:224
	s_waitcnt lgkmcnt(0)
	ds_read2_b32 v[20:21], v231 offset1:32
	ds_read2_b32 v[22:23], v231 offset0:64 offset1:96
	ds_read2_b32 v[24:25], v231 offset0:128 offset1:160
	ds_read2_b32 v[26:27], v231 offset0:192 offset1:224
	ds_read2_b32 v[28:29], v235 offset1:32
	ds_read2_b32 v[30:31], v235 offset0:64 offset1:96
	ds_read2_b32 v[32:33], v235 offset0:128 offset1:160
	ds_read2_b32 v[34:35], v235 offset0:192 offset1:224
	v_pk_mul_f32 v[4:5], v[4:5], v[214:215]
	v_pk_mul_f32 v[6:7], v[6:7], v[216:217]
	v_pk_mul_f32 v[8:9], v[8:9], v[218:219]
	v_pk_mul_f32 v[10:11], v[10:11], v[220:221]
	v_pk_mul_f32 v[12:13], v[12:13], v[222:223]
	v_pk_mul_f32 v[14:15], v[14:15], v[224:225]
	v_pk_mul_f32 v[16:17], v[16:17], v[226:227]
	v_pk_mul_f32 v[18:19], v[18:19], v[228:229]
	v_cvt_pk_fp8_f32 v244, v4, v5
	v_cvt_pk_fp8_f32 v245, v8, v9
	v_cvt_pk_fp8_f32 v246, v12, v13
	v_cvt_pk_fp8_f32 v247, v16, v17
	v_cvt_pk_fp8_f32 v244, v6, v7 op_sel:[0,0,1]
	v_cvt_pk_fp8_f32 v245, v10, v11 op_sel:[0,0,1]
	v_cvt_pk_fp8_f32 v246, v14, v15 op_sel:[0,0,1]
	v_cvt_pk_fp8_f32 v247, v18, v19 op_sel:[0,0,1]
	s_nop 0
	global_store_dwordx4 v238, v[244:247], s[34:35] nt
	s_waitcnt lgkmcnt(0)
	ds_read2_b32 v[36:37], v232 offset1:32
	ds_read2_b32 v[38:39], v232 offset0:64 offset1:96
	ds_read2_b32 v[40:41], v232 offset0:128 offset1:160
	ds_read2_b32 v[42:43], v232 offset0:192 offset1:224
	ds_read2_b32 v[44:45], v236 offset1:32
	ds_read2_b32 v[46:47], v236 offset0:64 offset1:96
	ds_read2_b32 v[48:49], v236 offset0:128 offset1:160
	ds_read2_b32 v[50:51], v236 offset0:192 offset1:224
	v_pk_mul_f32 v[20:21], v[20:21], v[214:215]
	v_pk_mul_f32 v[22:23], v[22:23], v[216:217]
	v_pk_mul_f32 v[24:25], v[24:25], v[218:219]
	v_pk_mul_f32 v[26:27], v[26:27], v[220:221]
	v_pk_mul_f32 v[28:29], v[28:29], v[222:223]
	v_pk_mul_f32 v[30:31], v[30:31], v[224:225]
	v_pk_mul_f32 v[32:33], v[32:33], v[226:227]
	v_pk_mul_f32 v[34:35], v[34:35], v[228:229]
	v_cvt_pk_fp8_f32 v244, v20, v21
	v_cvt_pk_fp8_f32 v245, v24, v25
	v_cvt_pk_fp8_f32 v246, v28, v29
	v_cvt_pk_fp8_f32 v247, v32, v33
	v_cvt_pk_fp8_f32 v244, v22, v23 op_sel:[0,0,1]
	v_cvt_pk_fp8_f32 v245, v26, v27 op_sel:[0,0,1]
	v_cvt_pk_fp8_f32 v246, v30, v31 op_sel:[0,0,1]
	v_cvt_pk_fp8_f32 v247, v34, v35 op_sel:[0,0,1]
	s_nop 0
	global_store_dwordx4 v239, v[244:247], s[34:35] nt
	s_waitcnt lgkmcnt(0)
	ds_read2_b32 v[52:53], v233 offset1:32
	ds_read2_b32 v[54:55], v233 offset0:64 offset1:96
	ds_read2_b32 v[56:57], v233 offset0:128 offset1:160
	ds_read2_b32 v[58:59], v233 offset0:192 offset1:224
	ds_read2_b32 v[60:61], v237 offset1:32
	ds_read2_b32 v[62:63], v237 offset0:64 offset1:96
	ds_read2_b32 v[64:65], v237 offset0:128 offset1:160
	ds_read2_b32 v[66:67], v237 offset0:192 offset1:224
	v_pk_mul_f32 v[36:37], v[36:37], v[214:215]
	v_pk_mul_f32 v[38:39], v[38:39], v[216:217]
	v_pk_mul_f32 v[40:41], v[40:41], v[218:219]
	v_pk_mul_f32 v[42:43], v[42:43], v[220:221]
	v_pk_mul_f32 v[44:45], v[44:45], v[222:223]
	v_pk_mul_f32 v[46:47], v[46:47], v[224:225]
	v_pk_mul_f32 v[48:49], v[48:49], v[226:227]
	v_pk_mul_f32 v[50:51], v[50:51], v[228:229]
	v_cvt_pk_fp8_f32 v244, v36, v37
	v_cvt_pk_fp8_f32 v245, v40, v41
	v_cvt_pk_fp8_f32 v246, v44, v45
	v_cvt_pk_fp8_f32 v247, v48, v49
	v_cvt_pk_fp8_f32 v244, v38, v39 op_sel:[0,0,1]
	v_cvt_pk_fp8_f32 v245, v42, v43 op_sel:[0,0,1]
	v_cvt_pk_fp8_f32 v246, v46, v47 op_sel:[0,0,1]
	v_cvt_pk_fp8_f32 v247, v50, v51 op_sel:[0,0,1]
	s_nop 0
	global_store_dwordx4 v240, v[244:247], s[34:35] nt
	s_waitcnt lgkmcnt(0)
	v_pk_mul_f32 v[52:53], v[52:53], v[214:215]
	v_pk_mul_f32 v[54:55], v[54:55], v[216:217]
	v_pk_mul_f32 v[56:57], v[56:57], v[218:219]
	v_pk_mul_f32 v[58:59], v[58:59], v[220:221]
	v_pk_mul_f32 v[60:61], v[60:61], v[222:223]
	v_pk_mul_f32 v[62:63], v[62:63], v[224:225]
	v_pk_mul_f32 v[64:65], v[64:65], v[226:227]
	v_pk_mul_f32 v[66:67], v[66:67], v[228:229]
	v_cvt_pk_fp8_f32 v244, v52, v53
	v_cvt_pk_fp8_f32 v245, v56, v57
	v_cvt_pk_fp8_f32 v246, v60, v61
	v_cvt_pk_fp8_f32 v247, v64, v65
	v_cvt_pk_fp8_f32 v244, v54, v55 op_sel:[0,0,1]
	v_cvt_pk_fp8_f32 v245, v58, v59 op_sel:[0,0,1]
	v_cvt_pk_fp8_f32 v246, v62, v63 op_sel:[0,0,1]
	v_cvt_pk_fp8_f32 v247, v66, v67 op_sel:[0,0,1]
	s_nop 0
	global_store_dwordx4 v241, v[244:247], s[34:35] nt
	s_add_i32 s7, s4, s5
	s_cmp_lt_u32 s7, s6
	s_cbranch_scc0 .Lhlp_done
	s_add_i32 s7, s4, s60
	s_cmp_lt_u32 s7, s6
	s_cbranch_scc0 .Lhlp_skip_1
	s_sub_i32 s50, s7, 0x2480
	s_cmp_lt_u32 s50, 0x10000
	s_cbranch_scc0 .Lhlp_dn_k1
	s_lshr_b32 s51, s50, 11
	s_bfe_u32 s52, s50, 0x40007
	s_and_b32 s53, s50, 0x7f
	s_lshl_b32 s54, s53, 5
	s_lshl_b32 s55, s51, 25
	s_lshl_b32 s56, s52, 21
	s_add_u32 s55, s55, s56
	s_lshl_b32 s56, s54, 2
	s_add_u32 s55, s55, s56
	s_add_u32 s8, s12, s55
	s_addc_u32 s9, s13, 0
	s_mov_b32 s10, 0x20000
	s_bfe_u32 s56, s53, 0x40002
	s_lshl_b32 s56, s56, 8
	s_and_b32 s57, s53, 3
	s_lshl_b32 s57, s57, 5
	s_add_u32 s56, s56, s57
	s_lshr_b32 s57, s53, 6
	s_lshl_b32 s57, s57, 7
	s_add_u32 s56, s56, s57
	s_lshl_b32 s56, s56, 11
	s_lshl_b32 s57, s51, 23
	s_add_u32 s56, s56, s57
	s_lshl_b32 s57, s52, 7
	s_add_u32 s56, s56, s57
	s_add_u32 s34, s16, s56
	s_addc_u32 s35, s17, 0
	s_lshl_b32 s57, s52, 9
	s_add_u32 s36, s57, 0x21800
	s_mov_b32 s37, -1
	v_mov_b32_e32 v211, v200
	s_branch .Lhlp_ld_k1

; #define GAS __attribute__((address_space(1)))
; __device__ __forceinline__ void tr_load(const TrItem& d, f32x4 (&v)[16], int lane) {
;     const int g = lane & 7, r0 = lane >> 3;
; #pragma unroll
;     for (int i = 0; i < 8; ++i) v[i] = __builtin_nontemporal_load((const GAS f32x4*)(d.W + (size_t)(d.k0 + r0 + 8 * i) * d.N + d.n0 + 4 * g));
;     if (d.is8) {
; #pragma unroll
;         for (int i = 8; i < 16; ++i) v[i] = __builtin_nontemporal_load((const GAS f32x4*)(d.W + (size_t)(d.k0 + r0 + 8 * i) * d.N + d.n0 + 4 * g)); }
; }
.Lhlp_ld_k1:
	global_load_dwordx4 v[4:7], v211, s[8:9] nt
	v_add_u32_e32 v211, s10, v211
	global_load_dwordx4 v[8:11], v211, s[8:9] nt
	v_add_u32_e32 v211, s10, v211
	global_load_dwordx4 v[12:15], v211, s[8:9] nt
	v_add_u32_e32 v211, s10, v211
	global_load_dwordx4 v[16:19], v211, s[8:9] nt
	v_add_u32_e32 v211, s10, v211
	global_load_dwordx4 v[20:23], v211, s[8:9] nt
	v_add_u32_e32 v211, s10, v211
	global_load_dwordx4 v[24:27], v211, s[8:9] nt
	v_add_u32_e32 v211, s10, v211
	global_load_dwordx4 v[28:31], v211, s[8:9] nt
	v_add_u32_e32 v211, s10, v211
	global_load_dwordx4 v[32:35], v211, s[8:9] nt
	v_add_u32_e32 v211, s10, v211
	global_load_dwordx4 v[36:39], v211, s[8:9] nt
	v_add_u32_e32 v211, s10, v211
	global_load_dwordx4 v[40:43], v211, s[8:9] nt
	v_add_u32_e32 v211, s10, v211
	global_load_dwordx4 v[44:47], v211, s[8:9] nt
	v_add_u32_e32 v211, s10, v211
	global_load_dwordx4 v[48:51], v211, s[8:9] nt
	v_add_u32_e32 v211, s10, v211
	global_load_dwordx4 v[52:55], v211, s[8:9] nt
	v_add_u32_e32 v211, s10, v211
	global_load_dwordx4 v[56:59], v211, s[8:9] nt
	v_add_u32_e32 v211, s10, v211
	global_load_dwordx4 v[60:63], v211, s[8:9] nt
	v_add_u32_e32 v211, s10, v211
	global_load_dwordx4 v[64:67], v211, s[8:9] nt
	s_branch .Lhlp_fin_1

; #define GAS __attribute__((address_space(1)))
; #define LAS __attribute__((address_space(3)))
; __device__ __forceinline__ unsigned pk4_fp8(float a, float b, float c, float d) { int w = 0; w = __builtin_amdgcn_cvt_pk_fp8_f32(a, b, w, false); w = __builtin_amdgcn_cvt_pk_fp8_f32(c, d, w, true); return (unsigned)w; }
; #define LDS_WAIT() asm volatile("s_waitcnt lgkmcnt(0)" ::: "memory")
; __device__ __forceinline__ void tr_finish(const TrItem& d, const f32x4 (&v)[16], LAS float* scr, int lane_) {
;     int lane = lane_; asm volatile("" : "+v"(lane));
;     const int c = lane & 7;
;     if (d.is8) {
;         { const int g = lane & 7, r0 = lane >> 3;
; #pragma unroll
;           for (int i = 0; i < 16; ++i) { const float gs = (d.gain ? d.gain[d.k0 + r0 + 8 * i] : 1.0f) * W8_SCALE; *(LAS f32x4*)(scr + (r0 + 8 * i) * 32 + ((g ^ (i >> 1)) << 2)) = v[i] * gs;
;               if ((i & 3) == 3) asm volatile("" ::: "memory"); } }
;         LDS_WAIT(); asm volatile("" ::: "memory");
; #pragma unroll
;         for (int j = 0; j < 4; ++j) { const int n = (lane >> 3) + 8 * j; const LAS float* s = scr + (16 * c) * 32 + ((((n >> 2) ^ c) << 2) + (n & 3));
;             v4u o; o.x = pk4_fp8(s[0 * 32], s[1 * 32], s[2 * 32], s[3 * 32]); o.y = pk4_fp8(s[4 * 32], s[5 * 32], s[6 * 32], s[7 * 32]); o.z = pk4_fp8(s[8 * 32], s[9 * 32], s[10 * 32], s[11 * 32]); o.w = pk4_fp8(s[12 * 32], s[13 * 32], s[14 * 32], s[15 * 32]);
;             __builtin_nontemporal_store(o, (GAS v4u*)(d.WT + (size_t)(d.drow0 + n) * d.K + d.k0 + 16 * c)); }
; __device__ __forceinline__ void p0_items(const P& p, LAS unsigned char* lds, int first, int last, int gw, int NGW, int wave, int lane) {
;     ...
;             if (it + 3 * st < last) { P0_DESC(d0, it + 3 * st); tr_load(d0, v0, lane); }
;             tr_finish(d1, v1, scr, lane);
;             if (it + 2 * st >= last) break;
;             if (it + 4 * st < last) { P0_DESC(d1, it + 4 * st); tr_load(d1, v1, lane); }
.Lhlp_fin_1:
	s_waitcnt vmcnt(32)
	ds_write_b128 v203, v[68:71]
	ds_write_b128 v203, v[72:75] offset:1024
	ds_write_b128 v204, v[76:79] offset:2048
	ds_write_b128 v204, v[80:83] offset:3072
	ds_write_b128 v205, v[84:87] offset:4096
	ds_write_b128 v205, v[88:91] offset:5120
	ds_write_b128 v206, v[92:95] offset:6144
	ds_write_b128 v206, v[96:99] offset:7168
	ds_write_b128 v207, v[100:103] offset:8192
	ds_write_b128 v207, v[104:107] offset:9216
	ds_write_b128 v208, v[108:111] offset:10240
	ds_write_b128 v208, v[112:115] offset:11264
	ds_write_b128 v209, v[116:119] offset:12288
	ds_write_b128 v209, v[120:123] offset:13312
	ds_write_b128 v210, v[124:127] offset:14336
	ds_write_b128 v210, v[128:131] offset:15360
	v_and_b32_e32 v242, s41, v202
	v_add_u32_e32 v242, s40, v242
	s_waitcnt lgkmcnt(0)
	ds_read_b128 v[214:217], v242
	ds_read_b128 v[218:221], v242 offset:16
	ds_read_b128 v[222:225], v242 offset:32
	ds_read_b128 v[226:229], v242 offset:48
	ds_read2_b32 v[68:69], v230 offset1:32
	ds_read2_b32 v[70:71], v230 offset0:64 offset1:96
	ds_read2_b32 v[72:73], v230 offset0:128 offset1:160
	ds_read2_b32 v[74:75], v230 offset0:192 offset1:224
	ds_read2_b32 v[76:77], v234 offset1:32
	ds_read2_b32 v[78:79], v234 offset0:64 offset1:96
	ds_read2_b32 v[80:81], v234 offset0:128 offset1:160
	ds_read2_b32 v[82:83], v234 offset0:192 offset1:224
	s_waitcnt lgkmcnt(0)
	ds_read2_b32 v[84:85], v231 offset1:32
	ds_read2_b32 v[86:87], v231 offset0:64 offset1:96
	ds_read2_b32 v[88:89], v231 offset0:128 offset1:160
	ds_read2_b32 v[90:91], v231 offset0:192 offset1:224
	ds_read2_b32 v[92:93], v235 offset1:32
	ds_read2_b32 v[94:95], v235 offset0:64 offset1:96
	ds_read2_b32 v[96:97], v235 offset0:128 offset1:160
	ds_read2_b32 v[98:99], v235 offset0:192 offset1:224
	v_pk_mul_f32 v[68:69], v[68:69], v[214:215]
	v_pk_mul_f32 v[70:71], v[70:71], v[216:217]
	v_pk_mul_f32 v[72:73], v[72:73], v[218:219]
	v_pk_mul_f32 v[74:75], v[74:75], v[220:221]
	v_pk_mul_f32 v[76:77], v[76:77], v[222:223]
	v_pk_mul_f32 v[78:79], v[78:79], v[224:225]
	v_pk_mul_f32 v[80:81], v[80:81], v[226:227]
	v_pk_mul_f32 v[82:83], v[82:83], v[228:229]
	v_cvt_pk_fp8_f32 v244, v68, v69
	v_cvt_pk_fp8_f32 v245, v72, v73
	v_cvt_pk_fp8_f32 v246, v76, v77
	v_cvt_pk_fp8_f32 v247, v80, v81
	v_cvt_pk_fp8_f32 v244, v70, v71 op_sel:[0,0,1]
	v_cvt_pk_fp8_f32 v245, v74, v75 op_sel:[0,0,1]
	v_cvt_pk_fp8_f32 v246, v78, v79 op_sel:[0,0,1]
	v_cvt_pk_fp8_f32 v247, v82, v83 op_sel:[0,0,1]
	s_nop 0
	global_store_dwordx4 v238, v[244:247], s[38:39] nt
	s_waitcnt lgkmcnt(0)
	ds_read2_b32 v[100:101], v232 offset1:32
	ds_read2_b32 v[102:103], v232 offset0:64 offset1:96
	ds_read2_b32 v[104:105], v232 offset0:128 offset1:160
	ds_read2_b32 v[106:107], v232 offset0:192 offset1:224
	ds_read2_b32 v[108:109], v236 offset1:32
	ds_read2_b32 v[110:111], v236 offset0:64 offset1:96
	ds_read2_b32 v[112:113], v236 offset0:128 offset1:160
	ds_read2_b32 v[114:115], v236 offset0:192 offset1:224
	v_pk_mul_f32 v[84:85], v[84:85], v[214:215]
	v_pk_mul_f32 v[86:87], v[86:87], v[216:217]
	v_pk_mul_f32 v[88:89], v[88:89], v[218:219]
	v_pk_mul_f32 v[90:91], v[90:91], v[220:221]
	v_pk_mul_f32 v[92:93], v[92:93], v[222:223]
	v_pk_mul_f32 v[94:95], v[94:95], v[224:225]
	v_pk_mul_f32 v[96:97], v[96:97], v[226:227]
	v_pk_mul_f32 v[98:99], v[98:99], v[228:229]
	v_cvt_pk_fp8_f32 v244, v84, v85
	v_cvt_pk_fp8_f32 v245, v88, v89
	v_cvt_pk_fp8_f32 v246, v92, v93
	v_cvt_pk_fp8_f32 v247, v96, v97
	v_cvt_pk_fp8_f32 v244, v86, v87 op_sel:[0,0,1]
	v_cvt_pk_fp8_f32 v245, v90, v91 op_sel:[0,0,1]
	v_cvt_pk_fp8_f32 v246, v94, v95 op_sel:[0,0,1]
	v_cvt_pk_fp8_f32 v247, v98, v99 op_sel:[0,0,1]
	s_nop 0
	global_store_dwordx4 v239, v[244:247], s[38:39] nt
	s_waitcnt lgkmcnt(0)
	ds_read2_b32 v[116:117], v233 offset1:32
	ds_read2_b32 v[118:119], v233 offset0:64 offset1:96
	ds_read2_b32 v[120:121], v233 offset0:128 offset1:160
	ds_read2_b32 v[122:123], v233 offset0:192 offset1:224
	ds_read2_b32 v[124:125], v237 offset1:32
	ds_read2_b32 v[126:127], v237 offset0:64 offset1:96
	ds_read2_b32 v[128:129], v237 offset0:128 offset1:160
	ds_read2_b32 v[130:131], v237 offset0:192 offset1:224
	v_pk_mul_f32 v[100:101], v[100:101], v[214:215]
	v_pk_mul_f32 v[102:103], v[102:103], v[216:217]
	v_pk_mul_f32 v[104:105], v[104:105], v[218:219]
	v_pk_mul_f32 v[106:107], v[106:107], v[220:221]
	v_pk_mul_f32 v[108:109], v[108:109], v[222:223]
	v_pk_mul_f32 v[110:111], v[110:111], v[224:225]
	v_pk_mul_f32 v[112:113], v[112:113], v[226:227]
	v_pk_mul_f32 v[114:115], v[114:115], v[228:229]
	v_cvt_pk_fp8_f32 v244, v100, v101
	v_cvt_pk_fp8_f32 v245, v104, v105
	v_cvt_pk_fp8_f32 v246, v108, v109
	v_cvt_pk_fp8_f32 v247, v112, v113
	v_cvt_pk_fp8_f32 v244, v102, v103 op_sel:[0,0,1]
	v_cvt_pk_fp8_f32 v245, v106, v107 op_sel:[0,0,1]
	v_cvt_pk_fp8_f32 v246, v110, v111 op_sel:[0,0,1]
	v_cvt_pk_fp8_f32 v247, v114, v115 op_sel:[0,0,1]
	s_nop 0
	global_store_dwordx4 v240, v[244:247], s[38:39] nt
	s_waitcnt lgkmcnt(0)
	v_pk_mul_f32 v[116:117], v[116:117], v[214:215]
	v_pk_mul_f32 v[118:119], v[118:119], v[216:217]
	v_pk_mul_f32 v[120:121], v[120:121], v[218:219]
	v_pk_mul_f32 v[122:123], v[122:123], v[220:221]
	v_pk_mul_f32 v[124:125], v[124:125], v[222:223]
	v_pk_mul_f32 v[126:127], v[126:127], v[224:225]
	v_pk_mul_f32 v[128:129], v[128:129], v[226:227]
	v_pk_mul_f32 v[130:131], v[130:131], v[228:229]
	v_cvt_pk_fp8_f32 v244, v116, v117
	v_cvt_pk_fp8_f32 v245, v120, v121
	v_cvt_pk_fp8_f32 v246, v124, v125
	v_cvt_pk_fp8_f32 v247, v128, v129
	v_cvt_pk_fp8_f32 v244, v118, v119 op_sel:[0,0,1]
	v_cvt_pk_fp8_f32 v245, v122, v123 op_sel:[0,0,1]
	v_cvt_pk_fp8_f32 v246, v126, v127 op_sel:[0,0,1]
	v_cvt_pk_fp8_f32 v247, v130, v131 op_sel:[0,0,1]
	s_nop 0
	global_store_dwordx4 v241, v[244:247], s[38:39] nt
	s_add_i32 s7, s4, s59
	s_cmp_lt_u32 s7, s6
	s_cbranch_scc0 .Lhlp_done
	s_add_i32 s7, s4, s61
	s_cmp_lt_u32 s7, s6
	s_cbranch_scc0 .Lhlp_skip_2
	s_sub_i32 s50, s7, 0x2480
	s_cmp_lt_u32 s50, 0x10000
	s_cbranch_scc0 .Lhlp_dn_k2
	s_lshr_b32 s51, s50, 11
	s_bfe_u32 s52, s50, 0x40007
	s_and_b32 s53, s50, 0x7f
	s_lshl_b32 s54, s53, 5
	s_lshl_b32 s55, s51, 25
	s_lshl_b32 s56, s52, 21
	s_add_u32 s55, s55, s56
	s_lshl_b32 s56, s54, 2
	s_add_u32 s55, s55, s56
	s_add_u32 s8, s12, s55
	s_addc_u32 s9, s13, 0
	s_mov_b32 s10, 0x20000
	s_bfe_u32 s56, s53, 0x40002
	s_lshl_b32 s56, s56, 8
	s_and_b32 s57, s53, 3
	s_lshl_b32 s57, s57, 5
	s_add_u32 s56, s56, s57
	s_lshr_b32 s57, s53, 6
	s_lshl_b32 s57, s57, 7
	s_add_u32 s56, s56, s57
	s_lshl_b32 s56, s56, 11
	s_lshl_b32 s57, s51, 23
	s_add_u32 s56, s56, s57
	s_lshl_b32 s57, s52, 7
	s_add_u32 s56, s56, s57
	s_add_u32 s38, s16, s56
	s_addc_u32 s39, s17, 0
	s_lshl_b32 s57, s52, 9
	s_add_u32 s40, s57, 0x21800
	s_mov_b32 s41, -1
	v_mov_b32_e32 v211, v200
	s_branch .Lhlp_ld_k2

; #define GAS __attribute__((address_space(1)))
; __device__ __forceinline__ void tr_load(const TrItem& d, f32x4 (&v)[16], int lane) {
;     const int g = lane & 7, r0 = lane >> 3;
; #pragma unroll
;     for (int i = 0; i < 8; ++i) v[i] = __builtin_nontemporal_load((const GAS f32x4*)(d.W + (size_t)(d.k0 + r0 + 8 * i) * d.N + d.n0 + 4 * g));
;     if (d.is8) {
; #pragma unroll
;         for (int i = 8; i < 16; ++i) v[i] = __builtin_nontemporal_load((const GAS f32x4*)(d.W + (size_t)(d.k0 + r0 + 8 * i) * d.N + d.n0 + 4 * g)); }
; }
.Lhlp_ld_k2:
	global_load_dwordx4 v[68:71], v211, s[8:9] nt
	v_add_u32_e32 v211, s10, v211
	global_load_dwordx4 v[72:75], v211, s[8:9] nt
	v_add_u32_e32 v211, s10, v211
	global_load_dwordx4 v[76:79], v211, s[8:9] nt
	v_add_u32_e32 v211, s10, v211
	global_load_dwordx4 v[80:83], v211, s[8:9] nt
	v_add_u32_e32 v211, s10, v211
	global_load_dwordx4 v[84:87], v211, s[8:9] nt
	v_add_u32_e32 v211, s10, v211
	global_load_dwordx4 v[88:91], v211, s[8:9] nt
	v_add_u32_e32 v211, s10, v211
	global_load_dwordx4 v[92:95], v211, s[8:9] nt
	v_add_u32_e32 v211, s10, v211
	global_load_dwordx4 v[96:99], v211, s[8:9] nt
	v_add_u32_e32 v211, s10, v211
	global_load_dwordx4 v[100:103], v211, s[8:9] nt
	v_add_u32_e32 v211, s10, v211
	global_load_dwordx4 v[104:107], v211, s[8:9] nt
	v_add_u32_e32 v211, s10, v211
	global_load_dwordx4 v[108:111], v211, s[8:9] nt
	v_add_u32_e32 v211, s10, v211
	global_load_dwordx4 v[112:115], v211, s[8:9] nt
	v_add_u32_e32 v211, s10, v211
	global_load_dwordx4 v[116:119], v211, s[8:9] nt
	v_add_u32_e32 v211, s10, v211
	global_load_dwordx4 v[120:123], v211, s[8:9] nt
	v_add_u32_e32 v211, s10, v211
	global_load_dwordx4 v[124:127], v211, s[8:9] nt
	v_add_u32_e32 v211, s10, v211
	global_load_dwordx4 v[128:131], v211, s[8:9] nt
	s_branch .Lhlp_fin_2

; #define GAS __attribute__((address_space(1)))
; #define LAS __attribute__((address_space(3)))
; __device__ __forceinline__ unsigned pk4_fp8(float a, float b, float c, float d) { int w = 0; w = __builtin_amdgcn_cvt_pk_fp8_f32(a, b, w, false); w = __builtin_amdgcn_cvt_pk_fp8_f32(c, d, w, true); return (unsigned)w; }
; #define LDS_WAIT() asm volatile("s_waitcnt lgkmcnt(0)" ::: "memory")
; __device__ __forceinline__ void tr_finish(const TrItem& d, const f32x4 (&v)[16], LAS float* scr, int lane_) {
;     int lane = lane_; asm volatile("" : "+v"(lane));
;     const int c = lane & 7;
;     if (d.is8) {
;         { const int g = lane & 7, r0 = lane >> 3;
; #pragma unroll
;           for (int i = 0; i < 16; ++i) { const float gs = (d.gain ? d.gain[d.k0 + r0 + 8 * i] : 1.0f) * W8_SCALE; *(LAS f32x4*)(scr + (r0 + 8 * i) * 32 + ((g ^ (i >> 1)) << 2)) = v[i] * gs;
;               if ((i & 3) == 3) asm volatile("" ::: "memory"); } }
;         LDS_WAIT(); asm volatile("" ::: "memory");
; #pragma unroll
;         for (int j = 0; j < 4; ++j) { const int n = (lane >> 3) + 8 * j; const LAS float* s = scr + (16 * c) * 32 + ((((n >> 2) ^ c) << 2) + (n & 3));
;             v4u o; o.x = pk4_fp8(s[0 * 32], s[1 * 32], s[2 * 32], s[3 * 32]); o.y = pk4_fp8(s[4 * 32], s[5 * 32], s[6 * 32], s[7 * 32]); o.z = pk4_fp8(s[8 * 32], s[9 * 32], s[10 * 32], s[11 * 32]); o.w = pk4_fp8(s[12 * 32], s[13 * 32], s[14 * 32], s[15 * 32]);
;             __builtin_nontemporal_store(o, (GAS v4u*)(d.WT + (size_t)(d.drow0 + n) * d.K + d.k0 + 16 * c)); }
; __device__ __forceinline__ void p0_items(const P& p, LAS unsigned char* lds, int first, int last, int gw, int NGW, int wave, int lane) {
;     ...
;             tr_finish(d2, v2, scr, lane);
;         }
;     }
.Lhlp_fin_2:
	s_waitcnt vmcnt(32)
	ds_write_b128 v203, v[132:135]
	ds_write_b128 v203, v[136:139] offset:1024
	ds_write_b128 v204, v[140:143] offset:2048
	ds_write_b128 v204, v[144:147] offset:3072
	ds_write_b128 v205, v[148:151] offset:4096
	ds_write_b128 v205, v[152:155] offset:5120
	ds_write_b128 v206, v[156:159] offset:6144
	ds_write_b128 v206, v[160:163] offset:7168
	ds_write_b128 v207, v[164:167] offset:8192
	ds_write_b128 v207, v[168:171] offset:9216
	ds_write_b128 v208, v[172:175] offset:10240
	ds_write_b128 v208, v[176:179] offset:11264
	ds_write_b128 v209, v[180:183] offset:12288
	ds_write_b128 v209, v[184:187] offset:13312
	ds_write_b128 v210, v[188:191] offset:14336
	ds_write_b128 v210, v[192:195] offset:15360
	v_and_b32_e32 v242, s49, v202
	v_add_u32_e32 v242, s48, v242
	s_waitcnt lgkmcnt(0)
	ds_read_b128 v[214:217], v242
	ds_read_b128 v[218:221], v242 offset:16
	ds_read_b128 v[222:225], v242 offset:32
	ds_read_b128 v[226:229], v242 offset:48
	ds_read2_b32 v[132:133], v230 offset1:32
	ds_read2_b32 v[134:135], v230 offset0:64 offset1:96
	ds_read2_b32 v[136:137], v230 offset0:128 offset1:160
	ds_read2_b32 v[138:139], v230 offset0:192 offset1:224
	ds_read2_b32 v[140:141], v234 offset1:32
	ds_read2_b32 v[142:143], v234 offset0:64 offset1:96
	ds_read2_b32 v[144:145], v234 offset0:128 offset1:160
	ds_read2_b32 v[146:147], v234 offset0:192 offset1:224
	s_waitcnt lgkmcnt(0)
	ds_read2_b32 v[148:149], v231 offset1:32
	ds_read2_b32 v[150:151], v231 offset0:64 offset1:96
	ds_read2_b32 v[152:153], v231 offset0:128 offset1:160
	ds_read2_b32 v[154:155], v231 offset0:192 offset1:224
	ds_read2_b32 v[156:157], v235 offset1:32
	ds_read2_b32 v[158:159], v235 offset0:64 offset1:96
	ds_read2_b32 v[160:161], v235 offset0:128 offset1:160
	ds_read2_b32 v[162:163], v235 offset0:192 offset1:224
	v_pk_mul_f32 v[132:133], v[132:133], v[214:215]
	v_pk_mul_f32 v[134:135], v[134:135], v[216:217]
	v_pk_mul_f32 v[136:137], v[136:137], v[218:219]
	v_pk_mul_f32 v[138:139], v[138:139], v[220:221]
	v_pk_mul_f32 v[140:141], v[140:141], v[222:223]
	v_pk_mul_f32 v[142:143], v[142:143], v[224:225]
	v_pk_mul_f32 v[144:145], v[144:145], v[226:227]
	v_pk_mul_f32 v[146:147], v[146:147], v[228:229]
	v_cvt_pk_fp8_f32 v244, v132, v133
	v_cvt_pk_fp8_f32 v245, v136, v137
	v_cvt_pk_fp8_f32 v246, v140, v141
	v_cvt_pk_fp8_f32 v247, v144, v145
	v_cvt_pk_fp8_f32 v244, v134, v135 op_sel:[0,0,1]
	v_cvt_pk_fp8_f32 v245, v138, v139 op_sel:[0,0,1]
	v_cvt_pk_fp8_f32 v246, v142, v143 op_sel:[0,0,1]
	v_cvt_pk_fp8_f32 v247, v146, v147 op_sel:[0,0,1]
	s_nop 0
	global_store_dwordx4 v238, v[244:247], s[46:47] nt
	s_waitcnt lgkmcnt(0)
	ds_read2_b32 v[164:165], v232 offset1:32
	ds_read2_b32 v[166:167], v232 offset0:64 offset1:96
	ds_read2_b32 v[168:169], v232 offset0:128 offset1:160
	ds_read2_b32 v[170:171], v232 offset0:192 offset1:224
	ds_read2_b32 v[172:173], v236 offset1:32
	ds_read2_b32 v[174:175], v236 offset0:64 offset1:96
	ds_read2_b32 v[176:177], v236 offset0:128 offset1:160
	ds_read2_b32 v[178:179], v236 offset0:192 offset1:224
	v_pk_mul_f32 v[148:149], v[148:149], v[214:215]
	v_pk_mul_f32 v[150:151], v[150:151], v[216:217]
	v_pk_mul_f32 v[152:153], v[152:153], v[218:219]
	v_pk_mul_f32 v[154:155], v[154:155], v[220:221]
	v_pk_mul_f32 v[156:157], v[156:157], v[222:223]
	v_pk_mul_f32 v[158:159], v[158:159], v[224:225]
	v_pk_mul_f32 v[160:161], v[160:161], v[226:227]
	v_pk_mul_f32 v[162:163], v[162:163], v[228:229]
	v_cvt_pk_fp8_f32 v244, v148, v149
	v_cvt_pk_fp8_f32 v245, v152, v153
	v_cvt_pk_fp8_f32 v246, v156, v157
	v_cvt_pk_fp8_f32 v247, v160, v161
	v_cvt_pk_fp8_f32 v244, v150, v151 op_sel:[0,0,1]
	v_cvt_pk_fp8_f32 v245, v154, v155 op_sel:[0,0,1]
	v_cvt_pk_fp8_f32 v246, v158, v159 op_sel:[0,0,1]
	v_cvt_pk_fp8_f32 v247, v162, v163 op_sel:[0,0,1]
	s_nop 0
	global_store_dwordx4 v239, v[244:247], s[46:47] nt
	s_waitcnt lgkmcnt(0)
	ds_read2_b32 v[180:181], v233 offset1:32
	ds_read2_b32 v[182:183], v233 offset0:64 offset1:96
	ds_read2_b32 v[184:185], v233 offset0:128 offset1:160
	ds_read2_b32 v[186:187], v233 offset0:192 offset1:224
	ds_read2_b32 v[188:189], v237 offset1:32
	ds_read2_b32 v[190:191], v237 offset0:64 offset1:96
	ds_read2_b32 v[192:193], v237 offset0:128 offset1:160
	ds_read2_b32 v[194:195], v237 offset0:192 offset1:224
	v_pk_mul_f32 v[164:165], v[164:165], v[214:215]
	v_pk_mul_f32 v[166:167], v[166:167], v[216:217]
	v_pk_mul_f32 v[168:169], v[168:169], v[218:219]
	v_pk_mul_f32 v[170:171], v[170:171], v[220:221]
	v_pk_mul_f32 v[172:173], v[172:173], v[222:223]
	v_pk_mul_f32 v[174:175], v[174:175], v[224:225]
	v_pk_mul_f32 v[176:177], v[176:177], v[226:227]
	v_pk_mul_f32 v[178:179], v[178:179], v[228:229]
	v_cvt_pk_fp8_f32 v244, v164, v165
	v_cvt_pk_fp8_f32 v245, v168, v169
	v_cvt_pk_fp8_f32 v246, v172, v173
	v_cvt_pk_fp8_f32 v247, v176, v177
	v_cvt_pk_fp8_f32 v244, v166, v167 op_sel:[0,0,1]
	v_cvt_pk_fp8_f32 v245, v170, v171 op_sel:[0,0,1]
	v_cvt_pk_fp8_f32 v246, v174, v175 op_sel:[0,0,1]
	v_cvt_pk_fp8_f32 v247, v178, v179 op_sel:[0,0,1]
	s_nop 0
	global_store_dwordx4 v240, v[244:247], s[46:47] nt
	s_waitcnt lgkmcnt(0)
	v_pk_mul_f32 v[180:181], v[180:181], v[214:215]
	v_pk_mul_f32 v[182:183], v[182:183], v[216:217]
	v_pk_mul_f32 v[184:185], v[184:185], v[218:219]
	v_pk_mul_f32 v[186:187], v[186:187], v[220:221]
	v_pk_mul_f32 v[188:189], v[188:189], v[222:223]
	v_pk_mul_f32 v[190:191], v[190:191], v[224:225]
	v_pk_mul_f32 v[192:193], v[192:193], v[226:227]
	v_pk_mul_f32 v[194:195], v[194:195], v[228:229]
	v_cvt_pk_fp8_f32 v244, v180, v181
	v_cvt_pk_fp8_f32 v245, v184, v185
	v_cvt_pk_fp8_f32 v246, v188, v189
	v_cvt_pk_fp8_f32 v247, v192, v193
	v_cvt_pk_fp8_f32 v244, v182, v183 op_sel:[0,0,1]
	v_cvt_pk_fp8_f32 v245, v186, v187 op_sel:[0,0,1]
	v_cvt_pk_fp8_f32 v246, v190, v191 op_sel:[0,0,1]
	v_cvt_pk_fp8_f32 v247, v194, v195 op_sel:[0,0,1]
	s_nop 0
	global_store_dwordx4 v241, v[244:247], s[46:47] nt
	s_add_i32 s4, s4, s60
	s_cmp_lt_u32 s4, s6
	s_cbranch_scc1 .Lhlp_loop
.Lhlp_done:
	s_waitcnt vmcnt(0) lgkmcnt(0)
	s_branch .LBB5_766
